# baseline (speedup 1.0000x reference)
_Z7k_stageILi0ELi4EEv8AttnArgsPKDF16_PKfPDF16_iii:
	s_load_dwordx16 s[64:79], s[0:1], 0x0
	v_readfirstlane_b32 s94, v0
	s_nop 0
	s_lshr_b32 s94, s94, 6
	s_cmp_lt_u32 s94, 4
	s_cbranch_scc1 .Lmyprio5
	s_setprio 1
.Lmyprio5:
	s_load_dwordx4 s[8:11], s[0:1], 0x70
	s_load_dwordx2 s[20:21], s[0:1], 0x80
	s_load_dwordx4 s[12:15], s[0:1], 0x88
	s_lshl_b32 s5, s2, 5
	s_waitcnt lgkmcnt(0)
	s_and_b32 s15, s5, 0xe0
	s_lshr_b32 s5, s2, 3
	s_add_i32 s15, s15, s5
	s_and_b32 s2, s2, 56
	v_readfirstlane_b32 s4, v0
	v_and_b32_e32 v1, 15, v0
	s_cmp_lt_i32 s14, 1
	v_bfe_u32 v158, v0, 4, 2
	s_cbranch_scc1 .LBB5_79
	s_bfe_u32 s5, s4, 0x10006
	s_lshl_b32 s6, s5, 4
	s_mul_i32 s16, s3, 40
	s_mul_hi_i32 s7, s3, 40
	s_add_u32 s22, s0, s16
	s_addc_u32 s23, s1, s7
	s_load_dwordx4 s[16:19], s[22:23], 0x0
	s_load_dwordx2 s[0:1], s[22:23], 0x10
	v_or_b32_e32 v159, s6, v1
	v_lshlrev_b32_e32 v18, 5, v159
	s_waitcnt lgkmcnt(0)
	global_load_dwordx4 v[230:233], v18, s[18:19]
	global_load_dwordx4 v[234:237], v18, s[0:1]
	global_load_dwordx4 v[238:241], v18, s[18:19] offset:16
	global_load_dwordx4 v[242:245], v18, s[0:1] offset:16
	v_bfe_u32 v21, v0, 7, 1
	v_lshrrev_b32_e32 v19, 4, v0
	v_lshlrev_b16_e32 v23, 2, v21
	v_lshrrev_b32_e32 v18, 5, v0
	v_lshrrev_b32_e32 v20, 6, v0
	v_and_b32_e32 v24, 3, v19
	v_bitop3_b16 v19, v23, v19, 3 bitop3:0xf8
	s_movk_i32 s0, 0x3000
	v_and_b32_e32 v18, 4, v18
	v_and_b32_e32 v22, 4, v20
	v_lshlrev_b32_e32 v20, 12, v20
	v_lshlrev_b32_e32 v21, 11, v21
	v_and_b32_e32 v19, 0xffff, v19
	s_bitcmp1_b32 s4, 6
	v_or_b32_e32 v161, v18, v158
	v_and_or_b32 v162, s15, 56, v22
	v_bitop3_b16 v23, v23, 8, v24 bitop3:0xfe
	v_lshlrev_b32_e32 v24, 3, v22
	v_lshl_or_b32 v22, v22, 12, v21
	v_or3_b32 v163, v20, v21, s0
	v_bitop3_b32 v18, v18, v159, v158 bitop3:0x36
	v_bitop3_b32 v19, s6, v19, v1 bitop3:0x36
	s_cselect_b64 s[24:25], -1, 0
	s_and_b32 s0, s15, 0x1ffc0
	s_movk_i32 s1, 0x2000
	v_lshl_or_b32 v168, v18, 4, v22
	v_lshlrev_b32_e32 v18, 4, v19
	v_or_b32_e32 v19, s0, v162
	v_add3_u32 v170, v22, v18, s1
	v_lshl_or_b32 v18, v19, 6, s2
	v_add_u32_e32 v18, v161, v18
	v_mul_u32_u24_e32 v18, 0x600, v18
	v_and_b32_e32 v20, 0xffff, v23
	v_lshl_or_b32 v18, s5, 8, v18
	v_lshlrev_b32_e32 v160, 9, v158
	v_bitop3_b32 v20, s6, v20, v1 bitop3:0x36
	v_lshl_or_b32 v18, v1, 4, v18
	v_add_u32_e32 v164, -1, v162
	v_add_u32_e32 v165, 4, v162
	v_or3_b32 v166, v161, v24, 8
	v_or_b32_e32 v167, 0x1000, v22
	v_lshl_or_b32 v169, v20, 4, v160
	s_and_b32 s17, s17, 0xffff
	s_mov_b32 s19, 0x20000
	s_mov_b32 s18, 0x1800000
	v_add_u32_e32 v171, 0xfffe7c00, v18
	s_mov_b32 s30, s2
	s_mov_b32 s93, 0
	s_branch .LBB5_4

.LBB5_79:
	s_setprio 0
	s_mul_i32 s0, s13, s3
	s_lshl_b32 s1, s15, 6
	s_add_i32 s0, s0, s12
	s_and_b32 s1, s1, 0xfffffe00
	s_or_b32 s6, s1, s2
	s_mul_i32 s2, s0, 0x60000
	s_mul_hi_i32 s1, s0, 0x60000
	s_add_u32 s2, s8, s2
	s_mulk_i32 s0, 0x300
	s_addc_u32 s7, s9, s1
	s_ashr_i32 s1, s0, 31
	s_lshl_b64 s[0:1], s[0:1], 2
	s_add_u32 s4, s10, s0
	s_addc_u32 s5, s11, s1
	s_mul_i32 s0, s3, 0x1800000
	s_mul_hi_i32 s1, s3, 0x1800000
	s_add_u32 s0, s20, s0
	v_readfirstlane_b32 s3, v0
	s_addc_u32 s1, s21, s1
	s_lshr_b32 s8, s3, 6
	s_and_b32 s1, s1, 0xffff
	s_mul_i32 s9, s8, 0x6000
	v_and_b32_e32 v2, 63, v0
	s_mul_hi_u32 s3, s8, 0x6000
	s_add_u32 s2, s2, s9
	s_addc_u32 s3, s7, s3
	v_lshlrev_b32_e32 v56, 4, v2
	v_mov_b32_e32 v57, 0
	v_lshl_add_u64 v[54:55], s[2:3], 0, v[56:57]
	s_movk_i32 s7, 0x1000
	v_add_co_u32_e32 v50, vcc, s7, v54
	s_movk_i32 s7, 0x2000
	s_nop 0
	v_addc_co_u32_e32 v51, vcc, 0, v55, vcc
	v_add_co_u32_e32 v52, vcc, s7, v54
	global_load_dwordx4 v[2:5], v56, s[2:3] offset:1024
	global_load_dwordx4 v[6:9], v56, s[2:3] offset:2048
	v_addc_co_u32_e32 v53, vcc, 0, v55, vcc
	global_load_dwordx4 v[10:13], v56, s[2:3] offset:3072
	global_load_dwordx4 v[14:17], v[52:53], off offset:-4096
	global_load_dwordx4 v[18:21], v[50:51], off offset:1024
	global_load_dwordx4 v[22:25], v[50:51], off offset:2048
	global_load_dwordx4 v[26:29], v56, s[2:3]
	global_load_dwordx4 v[30:33], v[50:51], off offset:3072
	global_load_dwordx4 v[34:37], v[52:53], off
	global_load_dwordx4 v[38:41], v[52:53], off offset:1024
	global_load_dwordx4 v[42:45], v[52:53], off offset:2048
	global_load_dwordx4 v[46:49], v[52:53], off offset:3072
	s_movk_i32 s2, 0x3000
	v_add_co_u32_e32 v58, vcc, s2, v54
	s_movk_i32 s2, 0x4000
	s_nop 0
	v_addc_co_u32_e32 v59, vcc, 0, v55, vcc
	v_add_co_u32_e32 v140, vcc, s2, v54
	s_waitcnt lgkmcnt(0)
	s_nop 0
	v_addc_co_u32_e32 v141, vcc, 0, v55, vcc
	s_barrier
	s_cmp_lt_u32 s94, 4
	s_cbranch_scc1 .Lmystag5_1
	s_sleep 4

.Lmyprio6:
	v_readfirstlane_b32 s3, v0
	s_lshl_b32 s12, s3, 1
	v_lshlrev_b32_e32 v3, 3, v0
	s_and_b32 s12, s12, 0x80
	v_and_b32_e32 v3, 0x78, v3
	s_load_dwordx4 s[8:11], s[0:1], 0x0
	s_load_dwordx2 s[4:5], s[0:1], 0x10
	s_load_dwordx2 s[6:7], s[0:1], 0x50
	v_or_b32_e32 v180, s12, v3
	s_lshl_b32 s12, s2, 5
	v_lshrrev_b32_e32 v1, 5, v0
	v_bfe_u32 v2, v0, 4, 2
	s_and_b32 s14, s12, 0xe0
	s_lshr_b32 s12, s2, 3
	v_lshrrev_b32_e32 v0, 6, v0
	v_and_b32_e32 v1, 4, v1
	s_add_i32 s14, s14, s12
	s_and_b32 s2, s2, 56
	v_and_b32_e32 v0, 4, v0
	v_and_or_b32 v181, s14, 56, v0
	v_or3_b32 v182, v2, s2, v1
	s_and_b32 s2, s14, 0x3ffffc0
	v_or_b32_e32 v4, s2, v181
	v_lshlrev_b32_e32 v0, 1, v180
	v_mov_b32_e32 v1, 0
	s_waitcnt lgkmcnt(0)
	v_lshl_add_u64 v[2:3], s[6:7], 0, v[0:1]
	v_lshl_or_b32 v0, v4, 6, v182
	v_lshlrev_b64 v[4:5], 9, v[0:1]
	v_lshl_add_u64 v[8:9], v[2:3], 0, v[4:5]
	v_or_b32_e32 v4, 64, v0
	v_mov_b32_e32 v5, v1
	v_lshlrev_b64 v[4:5], 9, v[4:5]
	v_lshlrev_b32_e32 v20, 2, v180
	v_lshl_add_u64 v[10:11], v[2:3], 0, v[4:5]
	global_load_dwordx4 v[240:243], v20, s[10:11] offset:16
	global_load_dwordx4 v[236:239], v20, s[10:11]
	global_load_dwordx4 v[248:251], v20, s[4:5] offset:16
	global_load_dwordx4 v[244:247], v20, s[4:5]
	global_load_dwordx4 v[12:15], v[8:9], off nt
	global_load_dwordx4 v[4:7], v[10:11], off nt
	v_or_b32_e32 v8, 0x80, v0
	v_mov_b32_e32 v9, v1
	v_lshlrev_b64 v[8:9], 9, v[8:9]
	v_or_b32_e32 v0, 0xc0, v0
	v_lshl_add_u64 v[20:21], v[2:3], 0, v[8:9]
	v_lshlrev_b64 v[0:1], 9, v[0:1]
	v_lshl_add_u64 v[34:35], v[2:3], 0, v[0:1]
	global_load_dwordx4 v[8:11], v[20:21], off nt
	global_load_dwordx4 v[0:3], v[34:35], off nt
	s_bitcmp1_b32 s3, 6
	s_cselect_b64 s[4:5], -1, 0
	s_and_b32 s2, s14, 0x3ffc0
	v_or_b32_e32 v20, s2, v181
	v_lshl_or_b32 v20, v20, 6, v182
	v_add_u32_e32 v184, -1, v182
	v_add_u32_e32 v185, -1, v181
	v_mul_u32_u24_e32 v20, 0x300, v20
	v_or_b32_e32 v34, v185, v184
	v_or_b32_e32 v20, v180, v20
	s_mov_b32 s11, 0x20000
	s_mov_b32 s10, 0x1800000
	s_and_b32 s9, s9, 0xffff
	v_lshlrev_b32_e32 v183, 1, v20
	v_cmp_gt_u32_e64 s[2:3], 64, v34
	s_and_b64 vcc, exec, s[4:5]
	s_cbranch_vccz .LBB6_38
	s_load_dwordx2 s[12:13], s[0:1], 0x20
	s_waitcnt lgkmcnt(0)
	s_load_dwordx2 s[4:5], s[12:13], 0x0
	s_load_dword s12, s[12:13], 0x8
	v_cmp_lt_u32_e64 s[64:65], 0, v182
	v_cmp_gt_u32_e64 s[66:67], 63, v182
	v_cmp_lt_u32_e64 s[68:69], 0, v181
	v_cmp_gt_u32_e64 s[70:71], 60, v181
	buffer_load_dwordx4 v[190:193], v183, s[8:11], 0 offen
	s_and_b64 s[72:73], s[68:69], s[64:65]
	s_and_b64 s[74:75], s[68:69], s[66:67]
	s_and_b64 s[76:77], s[70:71], s[64:65]
	s_and_b64 s[78:79], s[70:71], s[66:67]
	v_add_u32_e32 v228, 0xfffe7c00, v183
	v_add_u32_e32 v229, 0xfffe8000, v183
	s_mov_b64 exec, s[72:73]
	buffer_load_dwordx4 v[136:139], v228, s[8:11], 0 offen
	buffer_load_dwordx4 v[96:99], v228, s[8:11], 0 offen offset:512
	s_mov_b64 exec, -1
	s_mov_b64 exec, s[68:69]
	buffer_load_dwordx4 v[152:155], v229, s[8:11], 0 offen offset:512
	buffer_load_dwordx4 v[124:127], v229, s[8:11], 0 offen offset:1024
	s_mov_b64 exec, -1
	s_mov_b64 exec, s[74:75]
	buffer_load_dwordx4 v[160:163], v229, s[8:11], 0 offen offset:2048
	buffer_load_dwordx4 v[140:143], v229, s[8:11], 0 offen offset:2560
	s_mov_b64 exec, -1
	v_add_u32_e32 v228, 0xfffffc00, v183
	s_mov_b64 exec, s[64:65]
	buffer_load_dwordx4 v[112:115], v228, s[8:11], 0 offen
	buffer_load_dwordx4 v[68:71], v228, s[8:11], 0 offen offset:512
	s_mov_b64 exec, -1
	buffer_load_dwordx4 v[132:135], v183, s[8:11], 0 offen offset:512
	buffer_load_dwordx4 v[88:91], v183, s[8:11], 0 offen offset:1024
	s_mov_b64 exec, s[66:67]
	buffer_load_dwordx4 v[148:151], v183, s[8:11], 0 offen offset:2048
	buffer_load_dwordx4 v[108:111], v183, s[8:11], 0 offen offset:2560
	s_mov_b64 exec, -1
	v_add_u32_e32 v228, 0x17c00, v183
	v_add_u32_e32 v229, 0x18000, v183
	s_mov_b64 exec, s[64:65]
	buffer_load_dwordx4 v[76:79], v228, s[8:11], 0 offen
	buffer_load_dwordx4 v[48:51], v228, s[8:11], 0 offen offset:512
	s_mov_b64 exec, -1
	buffer_load_dwordx4 v[92:95], v229, s[8:11], 0 offen offset:512
	buffer_load_dwordx4 v[56:59], v229, s[8:11], 0 offen offset:1024
	s_mov_b64 exec, s[66:67]
	buffer_load_dwordx4 v[116:119], v229, s[8:11], 0 offen offset:2048
	buffer_load_dwordx4 v[72:75], v229, s[8:11], 0 offen offset:2560
	s_mov_b64 exec, -1
	v_add_u32_e32 v228, 0x18000, v183
	buffer_load_dwordx4 v[176:179], v228, s[8:11], 0 offen
	v_add_u32_e32 v229, 0x30000, v183
	buffer_load_dwordx4 v[172:175], v229, s[8:11], 0 offen
	v_add_u32_e32 v228, 0x48000, v183
	buffer_load_dwordx4 v[168:171], v228, s[8:11], 0 offen
	v_add_u32_e32 v228, 0x2fc00, v183
	v_add_u32_e32 v229, 0x30000, v183
	v_add_u32_e32 v230, 0x47c00, v183
	v_add_u32_e32 v231, 0x48000, v183
	v_add_u32_e32 v232, 0x5fc00, v183
	v_add_u32_e32 v233, 0x60000, v183
	s_waitcnt vmcnt(26)
	v_cvt_pk_f16_f32 v22, v240, v241
	v_cvt_pk_f16_f32 v20, v236, v237
	v_cvt_pk_f16_f32 v21, v238, v239
	v_cvt_pk_f16_f32 v16, v244, v245
	v_cvt_pk_f16_f32 v17, v246, v247
	v_cvt_pk_f16_f32 v18, v248, v249
	v_cvt_pk_f16_f32 v23, v242, v243
	v_cvt_pk_f16_f32 v19, v250, v251
	s_not_b64 exec, s[72:73]
	s_cbranch_execz .Lmyf_E1_0
	v_mov_b32_e32 v136, v20
	v_mov_b32_e32 v137, v21
	v_mov_b32_e32 v138, v22
	v_mov_b32_e32 v139, v23
	v_mov_b32_e32 v96, v16
	v_mov_b32_e32 v97, v17
	v_mov_b32_e32 v98, v18
	v_mov_b32_e32 v99, v19
